# vaccH LDS half: expert-id extraction by one SDWA shift (22+32 pairs) on top of the S5 latency fixes
# baseline (speedup 1.0000x reference)
; #define VL_LOAD(wr, C) do { _Pragma("unroll") for (int i = 0; i < 16; ++i) wr[i] = wp[(size_t)((C) * 16 + i) * MROWS]; } while (0)
; #define VL_LOAD(wr, C) do { _Pragma("unroll") for (int i = 0; i < 16; ++i) wr[i] = wp[(size_t)((C) * 16 + i) * MROWS]; } while (0)
; template <bool RUN_L = true, bool RUN_G = true, bool DRY = false>
; __device__ __forceinline__ void phase_vaccH(unsigned char* ws, LAS unsigned char* lds, int layer, int G) {
;     ...
;                 VL_LOAD(wa, 0);
; #pragma unroll 1
;                 for (int c = 0; c < 8; c += 2) {
;                     VL_LOAD(wb, c + 1);
;                     __builtin_amdgcn_sched_barrier(0);
;                     VL_CHUNK(wa);
.LBB0_1242:
	global_load_dword v24, v238, s[76:77]
	s_add_u32 s78, s76, s62
	s_addc_u32 s79, s77, 0
	global_load_dword v31, v238, s[78:79] offset:64
	v_mov_b32_e32 v19, v29
	s_add_u32 s78, s76, s56
	s_addc_u32 s79, s77, 0
	global_load_dword v30, v238, s[78:79] offset:128
	v_mov_b32_e32 v18, v28
	s_add_u32 s78, s76, s57
	s_addc_u32 s79, s77, 0
	global_load_dword v29, v238, s[78:79] offset:192
	v_mov_b32_e32 v17, v35
	s_add_u32 s78, s76, s64
	s_addc_u32 s79, s77, 0
	global_load_dword v28, v238, s[78:79] offset:256
	v_mov_b32_e32 v16, v34
	s_add_u32 s78, s76, s65
	s_addc_u32 s79, s77, 0
	global_load_dword v27, v238, s[78:79] offset:320
	s_add_u32 s78, s76, s66
	s_addc_u32 s79, s77, 0
	global_load_dword v26, v238, s[78:79] offset:384
	s_add_u32 s78, s76, s67
	s_addc_u32 s79, s77, 0
	global_load_dword v25, v238, s[78:79] offset:448
	s_add_u32 s78, s76, s68
	s_addc_u32 s79, s77, 0
	global_load_dword v54, v238, s[78:79] offset:512
	s_add_u32 s78, s76, s69
	s_addc_u32 s79, s77, 0
	global_load_dword v53, v238, s[78:79] offset:576
	s_add_u32 s78, s76, s70
	s_addc_u32 s79, s77, 0
	global_load_dword v52, v238, s[78:79] offset:640
	s_add_u32 s78, s76, s71
	s_addc_u32 s79, s77, 0
	global_load_dword v35, v238, s[78:79] offset:704
	s_add_u32 s78, s76, s72
	s_addc_u32 s79, s77, 0
	global_load_dword v34, v238, s[78:79] offset:768
	s_add_u32 s78, s76, s73
	s_addc_u32 s79, s77, 0
	global_load_dword v33, v238, s[78:79] offset:832
	s_add_u32 s78, s76, s74
	s_addc_u32 s79, s77, 0
	global_load_dword v32, v238, s[78:79] offset:896
	s_add_u32 s78, s76, s75
	s_addc_u32 s79, s77, 0
	global_load_dword v55, v238, s[78:79] offset:960
	s_waitcnt vmcnt(30)
	v_lshlrev_b32_sdwa v58, v239, v37 dst_sel:DWORD dst_unused:UNUSED_PAD src0_sel:DWORD src1_sel:WORD_1
	s_waitcnt vmcnt(29)
	v_lshlrev_b32_sdwa v60, v239, v38 dst_sel:DWORD dst_unused:UNUSED_PAD src0_sel:DWORD src1_sel:WORD_1
	s_waitcnt vmcnt(28)
	v_lshlrev_b32_sdwa v56, v239, v36 dst_sel:DWORD dst_unused:UNUSED_PAD src0_sel:DWORD src1_sel:WORD_1
	v_lshlrev_b32_sdwa v62, v239, v39 dst_sel:DWORD dst_unused:UNUSED_PAD src0_sel:DWORD src1_sel:WORD_1
	ds_read_b64 v[56:57], v56
	ds_read_b64 v[58:59], v58
	ds_read_b64 v[60:61], v60
	ds_read_b64 v[62:63], v62
	v_perm_b32 v36, v36, v36, s63
	s_waitcnt lgkmcnt(3)
	v_perm_b32 v88, 0, v56, v169
	v_perm_b32 v56, 0, v56, v170
	v_perm_b32 v89, 0, v57, v169
	v_perm_b32 v57, 0, v57, v170
	v_pk_fma_f16 v88, v36, v88, 0
	v_pk_fma_f16 v56, v36, v56, 0
	v_pk_fma_f16 v89, v36, v89, 0
	v_pk_fma_f16 v36, v36, v57, 0
	v_perm_b32 v37, v37, v37, s63
	s_waitcnt lgkmcnt(2)
	v_perm_b32 v57, 0, v58, v169
	v_perm_b32 v58, 0, v58, v170
	v_pk_fma_f16 v56, v37, v58, v56
	v_perm_b32 v58, 0, v59, v169
	v_perm_b32 v59, 0, v59, v170
	v_pk_fma_f16 v57, v37, v57, v88
	v_pk_fma_f16 v58, v37, v58, v89
	v_pk_fma_f16 v36, v37, v59, v36
	v_perm_b32 v37, v38, v38, s63
	s_waitcnt lgkmcnt(1)
	v_perm_b32 v38, 0, v60, v169
	v_pk_fma_f16 v38, v37, v38, v57
	v_perm_b32 v57, 0, v60, v170
	s_waitcnt vmcnt(26)
	v_pk_fma_f16 v56, v37, v57, v56
	v_perm_b32 v57, 0, v61, v169
	v_lshlrev_b32_sdwa v66, v239, v41 dst_sel:DWORD dst_unused:UNUSED_PAD src0_sel:DWORD src1_sel:WORD_1
	s_waitcnt vmcnt(25)
	v_pk_fma_f16 v57, v37, v57, v58
	v_perm_b32 v58, 0, v61, v170
	v_lshlrev_b32_sdwa v68, v239, v42 dst_sel:DWORD dst_unused:UNUSED_PAD src0_sel:DWORD src1_sel:WORD_1
	s_waitcnt vmcnt(24)
	v_pk_fma_f16 v36, v37, v58, v36
	v_perm_b32 v37, v39, v39, s63
	s_waitcnt lgkmcnt(0)
	v_perm_b32 v39, 0, v62, v169
	v_lshlrev_b32_sdwa v64, v239, v40 dst_sel:DWORD dst_unused:UNUSED_PAD src0_sel:DWORD src1_sel:WORD_1
	v_lshlrev_b32_sdwa v70, v239, v44 dst_sel:DWORD dst_unused:UNUSED_PAD src0_sel:DWORD src1_sel:WORD_1
	v_pk_fma_f16 v38, v37, v39, v38
	v_perm_b32 v39, 0, v62, v170
	ds_read_b64 v[64:65], v64
	ds_read_b64 v[66:67], v66
	ds_read_b64 v[68:69], v68
	ds_read_b64 v[70:71], v70
	v_pk_fma_f16 v39, v37, v39, v56
	v_perm_b32 v56, 0, v63, v169
	v_pk_fma_f16 v56, v37, v56, v57
	v_perm_b32 v57, 0, v63, v170
	v_pk_fma_f16 v36, v37, v57, v36
	v_perm_b32 v37, v40, v40, s63
	s_waitcnt lgkmcnt(3)
	v_perm_b32 v40, 0, v64, v169
	v_pk_fma_f16 v38, v37, v40, v38
	v_perm_b32 v40, 0, v64, v170
	v_pk_fma_f16 v39, v37, v40, v39
	v_perm_b32 v40, 0, v65, v169
	v_pk_fma_f16 v40, v37, v40, v56
	v_perm_b32 v56, 0, v65, v170
	v_pk_fma_f16 v36, v37, v56, v36
	v_perm_b32 v37, v41, v41, s63
	s_waitcnt lgkmcnt(2)
	v_perm_b32 v41, 0, v66, v169
	v_pk_fma_f16 v38, v37, v41, v38
	v_perm_b32 v41, 0, v66, v170
	v_pk_fma_f16 v39, v37, v41, v39
	v_perm_b32 v41, 0, v67, v169
	v_pk_fma_f16 v40, v37, v41, v40
	v_perm_b32 v41, 0, v67, v170
	v_pk_fma_f16 v36, v37, v41, v36
	v_perm_b32 v37, v42, v42, s63
	s_waitcnt lgkmcnt(1)
	v_perm_b32 v41, 0, v68, v169
	v_pk_fma_f16 v38, v37, v41, v38
	v_perm_b32 v41, 0, v68, v170
	s_waitcnt vmcnt(22)
	v_pk_fma_f16 v39, v37, v41, v39
	v_perm_b32 v41, 0, v69, v169
	v_lshlrev_b32_sdwa v74, v239, v45 dst_sel:DWORD dst_unused:UNUSED_PAD src0_sel:DWORD src1_sel:WORD_1
	s_waitcnt vmcnt(21)
	v_pk_fma_f16 v40, v37, v41, v40
	v_perm_b32 v41, 0, v69, v170
	v_lshlrev_b32_sdwa v76, v239, v46 dst_sel:DWORD dst_unused:UNUSED_PAD src0_sel:DWORD src1_sel:WORD_1
	s_waitcnt vmcnt(20)
	v_pk_fma_f16 v36, v37, v41, v36
	v_perm_b32 v37, v44, v44, s63
	s_waitcnt lgkmcnt(0)
	v_perm_b32 v41, 0, v70, v169
	v_lshlrev_b32_sdwa v72, v239, v43 dst_sel:DWORD dst_unused:UNUSED_PAD src0_sel:DWORD src1_sel:WORD_1
	v_lshlrev_b32_sdwa v78, v239, v47 dst_sel:DWORD dst_unused:UNUSED_PAD src0_sel:DWORD src1_sel:WORD_1
	v_pk_fma_f16 v38, v37, v41, v38
	v_perm_b32 v41, 0, v70, v170
	ds_read_b64 v[72:73], v72
	ds_read_b64 v[74:75], v74
	ds_read_b64 v[76:77], v76
	ds_read_b64 v[78:79], v78
	v_pk_fma_f16 v39, v37, v41, v39
	v_perm_b32 v41, 0, v71, v169
	v_pk_fma_f16 v40, v37, v41, v40
	v_perm_b32 v41, 0, v71, v170
	v_pk_fma_f16 v36, v37, v41, v36
	v_perm_b32 v37, v43, v43, s63
	s_waitcnt lgkmcnt(3)
; #define VL_LOAD(wr, C) do { _Pragma("unroll") for (int i = 0; i < 16; ++i) wr[i] = wp[(size_t)((C) * 16 + i) * MROWS]; } while (0)
; #define VL_LOAD(wr, C) do { _Pragma("unroll") for (int i = 0; i < 16; ++i) wr[i] = wp[(size_t)((C) * 16 + i) * MROWS]; } while (0)
; template <bool RUN_L = true, bool RUN_G = true, bool DRY = false>
; __device__ __forceinline__ void phase_vaccH(unsigned char* ws, LAS unsigned char* lds, int layer, int G) {
;     ...
;                     VL_LOAD(wa, (c + 2) & 7);
	v_perm_b32 v41, 0, v72, v169
	v_pk_fma_f16 v38, v37, v41, v38
	v_perm_b32 v41, 0, v72, v170
	v_pk_fma_f16 v39, v37, v41, v39
	v_perm_b32 v41, 0, v73, v169
	v_pk_fma_f16 v40, v37, v41, v40
	v_perm_b32 v41, 0, v73, v170
	v_pk_fma_f16 v36, v37, v41, v36
	v_perm_b32 v37, v45, v45, s63
	s_waitcnt lgkmcnt(2)
	v_perm_b32 v41, 0, v74, v169
	v_pk_fma_f16 v38, v37, v41, v38
	v_perm_b32 v41, 0, v74, v170
	v_pk_fma_f16 v39, v37, v41, v39
	v_perm_b32 v41, 0, v75, v169
	v_pk_fma_f16 v40, v37, v41, v40
	v_perm_b32 v41, 0, v75, v170
	v_pk_fma_f16 v36, v37, v41, v36
	v_perm_b32 v37, v46, v46, s63
	s_waitcnt lgkmcnt(1)
	v_perm_b32 v41, 0, v76, v169
	v_pk_fma_f16 v38, v37, v41, v38
	v_perm_b32 v41, 0, v76, v170
	s_waitcnt vmcnt(18)
	v_pk_fma_f16 v39, v37, v41, v39
	v_perm_b32 v41, 0, v77, v169
	v_lshlrev_b32_sdwa v82, v239, v49 dst_sel:DWORD dst_unused:UNUSED_PAD src0_sel:DWORD src1_sel:WORD_1
	s_waitcnt vmcnt(17)
	v_pk_fma_f16 v40, v37, v41, v40
	v_perm_b32 v41, 0, v77, v170
	v_lshlrev_b32_sdwa v84, v239, v50 dst_sel:DWORD dst_unused:UNUSED_PAD src0_sel:DWORD src1_sel:WORD_1
	s_waitcnt vmcnt(16)
	v_pk_fma_f16 v36, v37, v41, v36
	v_perm_b32 v37, v47, v47, s63
	s_waitcnt lgkmcnt(0)
	v_perm_b32 v41, 0, v78, v169
	v_lshlrev_b32_sdwa v80, v239, v48 dst_sel:DWORD dst_unused:UNUSED_PAD src0_sel:DWORD src1_sel:WORD_1
	v_lshlrev_b32_sdwa v86, v239, v51 dst_sel:DWORD dst_unused:UNUSED_PAD src0_sel:DWORD src1_sel:WORD_1
	v_pk_fma_f16 v38, v37, v41, v38
	v_perm_b32 v41, 0, v78, v170
	ds_read_b64 v[80:81], v80
	ds_read_b64 v[82:83], v82
	ds_read_b64 v[84:85], v84
	ds_read_b64 v[86:87], v86
	v_pk_fma_f16 v39, v37, v41, v39
	v_perm_b32 v41, 0, v79, v169
	v_pk_fma_f16 v40, v37, v41, v40
	v_perm_b32 v41, 0, v79, v170
	v_pk_fma_f16 v36, v37, v41, v36
	v_perm_b32 v37, v48, v48, s63
	s_waitcnt lgkmcnt(3)
	v_perm_b32 v41, 0, v80, v169
	v_pk_fma_f16 v38, v37, v41, v38
	v_perm_b32 v41, 0, v80, v170
	v_pk_fma_f16 v39, v37, v41, v39
	v_perm_b32 v41, 0, v81, v169
	v_pk_fma_f16 v40, v37, v41, v40
	v_perm_b32 v41, 0, v81, v170
	v_pk_fma_f16 v36, v37, v41, v36
	v_perm_b32 v37, v49, v49, s63
	s_waitcnt lgkmcnt(2)
	v_perm_b32 v41, 0, v82, v169
	v_pk_fma_f16 v38, v37, v41, v38
	v_perm_b32 v41, 0, v82, v170
	v_pk_fma_f16 v39, v37, v41, v39
	v_perm_b32 v41, 0, v83, v169
	v_pk_fma_f16 v40, v37, v41, v40
	v_perm_b32 v41, 0, v83, v170
	v_pk_fma_f16 v36, v37, v41, v36
	v_perm_b32 v37, v50, v50, s63
	s_waitcnt lgkmcnt(1)
	v_perm_b32 v41, 0, v84, v169
	v_pk_fma_f16 v38, v37, v41, v38
	v_perm_b32 v41, 0, v84, v170
	v_pk_fma_f16 v39, v37, v41, v39
	v_perm_b32 v41, 0, v85, v169
	v_pk_fma_f16 v40, v37, v41, v40
	v_perm_b32 v41, 0, v85, v170
	v_pk_fma_f16 v36, v37, v41, v36
	v_perm_b32 v37, v51, v51, s63
	s_waitcnt lgkmcnt(0)
	v_perm_b32 v41, 0, v86, v169
	v_pk_fma_f16 v58, v37, v41, v38
	v_perm_b32 v38, 0, v86, v170
	v_pk_fma_f16 v59, v37, v38, v39
	v_perm_b32 v38, 0, v87, v169
	v_pk_fma_f16 v60, v37, v38, v40
	v_perm_b32 v38, 0, v87, v170
	v_pk_fma_f16 v61, v37, v38, v36
	s_and_b32 s8, s46, 0x60
	s_mul_i32 s8, s8, 0x8040
	s_add_u32 s98, s16, s8
	s_addc_u32 s99, s17, 0
	global_load_dword v36, v238, s[98:99]
	s_add_u32 s78, s98, s62
	s_addc_u32 s79, s99, 0
	global_load_dword v37, v238, s[78:79] offset:64
	s_add_u32 s78, s98, s56
	s_addc_u32 s79, s99, 0
	global_load_dword v38, v238, s[78:79] offset:128
	s_add_u32 s78, s98, s57
	s_addc_u32 s79, s99, 0
	global_load_dword v39, v238, s[78:79] offset:192
	s_add_u32 s78, s98, s64
	s_addc_u32 s79, s99, 0
	global_load_dword v40, v238, s[78:79] offset:256
	s_add_u32 s78, s98, s65
	s_addc_u32 s79, s99, 0
	global_load_dword v41, v238, s[78:79] offset:320
	s_add_u32 s78, s98, s66
	s_addc_u32 s79, s99, 0
	global_load_dword v42, v238, s[78:79] offset:384
	s_add_u32 s78, s98, s67
	s_addc_u32 s79, s99, 0
	global_load_dword v44, v238, s[78:79] offset:448
	s_add_u32 s78, s98, s68
	s_addc_u32 s79, s99, 0
	global_load_dword v43, v238, s[78:79] offset:512
	s_add_u32 s78, s98, s69
	s_addc_u32 s79, s99, 0
	global_load_dword v45, v238, s[78:79] offset:576
	s_add_u32 s78, s98, s70
	s_addc_u32 s79, s99, 0
	global_load_dword v46, v238, s[78:79] offset:640
	s_add_u32 s78, s98, s71
	s_addc_u32 s79, s99, 0
	global_load_dword v47, v238, s[78:79] offset:704
	s_add_u32 s78, s98, s72
	s_addc_u32 s79, s99, 0
	global_load_dword v48, v238, s[78:79] offset:768
	s_add_u32 s78, s98, s73
	s_addc_u32 s79, s99, 0
	global_load_dword v49, v238, s[78:79] offset:832
	s_add_u32 s78, s98, s74
	s_addc_u32 s79, s99, 0
	global_load_dword v50, v238, s[78:79] offset:896
	s_add_u32 s78, s98, s75
	s_addc_u32 s79, s99, 0
	global_load_dword v51, v238, s[78:79] offset:960
	s_waitcnt vmcnt(30)
	v_bfe_u32 v57, v31, 16, 16
	s_waitcnt vmcnt(29)
	v_bfe_u32 v62, v30, 16, 16
	s_waitcnt vmcnt(28)
	v_bfe_u32 v63, v29, 16, 16
	s_waitcnt vmcnt(27)
	v_bfe_u32 v64, v28, 16, 16
	v_perm_b32 v85, v31, v31, s63
	v_perm_b32 v86, v30, v30, s63
	v_perm_b32 v87, v29, v29, s63
	v_perm_b32 v88, v28, v28, s63
	v_cvt_f32_f16_e32 v28, v60
	v_cvt_f32_f16_sdwa v29, v60 dst_sel:DWORD dst_unused:UNUSED_PAD src0_sel:WORD_1
	v_cvt_f32_f16_e32 v30, v61
	v_cvt_f32_f16_sdwa v31, v61 dst_sel:DWORD dst_unused:UNUSED_PAD src0_sel:WORD_1
	v_bfe_u32 v56, v24, 16, 16
	s_waitcnt vmcnt(26)
	s_waitcnt vmcnt(25)
	s_waitcnt vmcnt(24)
	v_bfe_u32 v67, v25, 16, 16
	s_waitcnt vmcnt(23)
	v_bfe_u32 v68, v54, 16, 16
	s_waitcnt vmcnt(22)
	s_waitcnt vmcnt(21)
	v_bfe_u32 v70, v52, 16, 16
	s_waitcnt vmcnt(20)
	s_waitcnt vmcnt(19)
	v_bfe_u32 v72, v34, 16, 16
	s_waitcnt vmcnt(18)
	s_waitcnt vmcnt(17)
	v_bfe_u32 v74, v32, 16, 16
	s_waitcnt vmcnt(16)
	v_perm_b32 v84, v24, v24, s63
	v_perm_b32 v91, v25, v25, s63
	v_perm_b32 v92, v54, v54, s63
	v_perm_b32 v94, v52, v52, s63
	v_perm_b32 v96, v34, v34, s63
	v_perm_b32 v98, v32, v32, s63
	v_cvt_f32_f16_e32 v24, v58
	v_cvt_f32_f16_sdwa v25, v58 dst_sel:DWORD dst_unused:UNUSED_PAD src0_sel:WORD_1
	v_lshl_add_u32 v32, v56, 3, 0
	v_lshl_add_u32 v34, v57, 3, 0
	v_lshl_add_u32 v52, v62, 3, 0
	v_lshl_add_u32 v54, v63, 3, 0
	v_lshl_add_u32 v56, v64, 3, 0
	v_lshlrev_b32_sdwa v58, v239, v27 dst_sel:DWORD dst_unused:UNUSED_PAD src0_sel:DWORD src1_sel:WORD_1
	v_lshlrev_b32_sdwa v60, v239, v26 dst_sel:DWORD dst_unused:UNUSED_PAD src0_sel:DWORD src1_sel:WORD_1
	v_lshl_add_u32 v62, v67, 3, 0
	v_lshl_add_u32 v64, v68, 3, 0
	v_lshlrev_b32_sdwa v66, v239, v53 dst_sel:DWORD dst_unused:UNUSED_PAD src0_sel:DWORD src1_sel:WORD_1
	v_lshl_add_u32 v68, v70, 3, 0
	v_lshlrev_b32_sdwa v70, v239, v35 dst_sel:DWORD dst_unused:UNUSED_PAD src0_sel:DWORD src1_sel:WORD_1
	v_lshl_add_u32 v72, v72, 3, 0
	v_lshlrev_b32_sdwa v76, v239, v33 dst_sel:DWORD dst_unused:UNUSED_PAD src0_sel:DWORD src1_sel:WORD_1
	v_lshl_add_u32 v77, v74, 3, 0
	v_lshlrev_b32_sdwa v78, v239, v55 dst_sel:DWORD dst_unused:UNUSED_PAD src0_sel:DWORD src1_sel:WORD_1
	v_perm_b32 v89, v27, v27, s63
	v_perm_b32 v90, v26, v26, s63
	v_perm_b32 v93, v53, v53, s63
	v_perm_b32 v95, v35, v35, s63
	v_perm_b32 v97, v33, v33, s63
	v_perm_b32 v99, v55, v55, s63
	v_cvt_f32_f16_e32 v26, v59
	v_cvt_f32_f16_sdwa v27, v59 dst_sel:DWORD dst_unused:UNUSED_PAD src0_sel:WORD_1
	ds_read_b64 v[32:33], v32
	ds_read_b64 v[34:35], v34
	ds_read_b64 v[52:53], v52
	ds_read_b64 v[54:55], v54
	ds_read_b64 v[56:57], v56
	ds_read_b64 v[58:59], v58
	ds_read_b64 v[60:61], v60
	ds_read_b64 v[62:63], v62
	ds_read_b64 v[64:65], v64
	ds_read_b64 v[66:67], v66
	ds_read_b64 v[68:69], v68
	ds_read_b64 v[70:71], v70
	ds_read_b64 v[72:73], v72
	ds_read_b64 v[74:75], v76
	ds_read_b64 v[76:77], v77
	ds_read_b64 v[78:79], v78
	v_pk_add_f32 v[22:23], v[22:23], v[28:29]
	v_pk_add_f32 v[20:21], v[20:21], v[30:31]
	s_waitcnt lgkmcnt(14)
	v_perm_b32 v28, 0, v32, v169
	v_perm_b32 v29, 0, v32, v170
	v_perm_b32 v30, 0, v33, v169
	v_perm_b32 v31, 0, v33, v170
	v_perm_b32 v32, 0, v34, v169
	v_perm_b32 v33, 0, v34, v170
	v_perm_b32 v34, 0, v35, v169
	v_perm_b32 v35, 0, v35, v170
	v_pk_fma_f16 v28, v84, v28, 0
	v_pk_fma_f16 v29, v84, v29, 0
	v_pk_fma_f16 v30, v84, v30, 0
	v_pk_fma_f16 v31, v84, v31, 0
	s_waitcnt lgkmcnt(13)
	v_perm_b32 v100, 0, v52, v169
	v_perm_b32 v52, 0, v52, v170
	v_perm_b32 v101, 0, v53, v169
	v_perm_b32 v53, 0, v53, v170
	v_pk_fma_f16 v28, v85, v32, v28
	v_pk_fma_f16 v29, v85, v33, v29
	v_pk_fma_f16 v30, v85, v34, v30
	v_pk_fma_f16 v31, v85, v35, v31
	s_waitcnt lgkmcnt(12)
	v_perm_b32 v102, 0, v54, v169
	v_perm_b32 v54, 0, v54, v170
	v_perm_b32 v103, 0, v55, v169
	v_perm_b32 v55, 0, v55, v170
	v_pk_fma_f16 v28, v86, v100, v28
	v_pk_fma_f16 v29, v86, v52, v29
	v_pk_fma_f16 v30, v86, v101, v30
	v_pk_fma_f16 v31, v86, v53, v31
	s_waitcnt lgkmcnt(11)
	v_perm_b32 v104, 0, v56, v169
	v_perm_b32 v56, 0, v56, v170
	v_perm_b32 v105, 0, v57, v169
	v_perm_b32 v57, 0, v57, v170
	v_pk_fma_f16 v28, v87, v102, v28
	v_pk_fma_f16 v29, v87, v54, v29
	v_pk_fma_f16 v30, v87, v103, v30
	v_pk_fma_f16 v31, v87, v55, v31
	s_waitcnt lgkmcnt(10)
	v_perm_b32 v106, 0, v58, v169
	v_perm_b32 v58, 0, v58, v170
	v_perm_b32 v107, 0, v59, v169
	v_perm_b32 v59, 0, v59, v170
	v_pk_fma_f16 v28, v88, v104, v28
	v_pk_fma_f16 v29, v88, v56, v29
	v_pk_fma_f16 v30, v88, v105, v30
	v_pk_fma_f16 v31, v88, v57, v31
	s_waitcnt lgkmcnt(9)
	v_perm_b32 v108, 0, v60, v169
	v_perm_b32 v60, 0, v60, v170
	v_perm_b32 v109, 0, v61, v169
	v_perm_b32 v61, 0, v61, v170
	v_pk_fma_f16 v28, v89, v106, v28
	v_pk_fma_f16 v29, v89, v58, v29
	v_pk_fma_f16 v30, v89, v107, v30
	v_pk_fma_f16 v31, v89, v59, v31
	s_waitcnt lgkmcnt(8)
; #define VL_LOAD(wr, C) do { _Pragma("unroll") for (int i = 0; i < 16; ++i) wr[i] = wp[(size_t)((C) * 16 + i) * MROWS]; } while (0)
; #define VL_LOAD(wr, C) do { _Pragma("unroll") for (int i = 0; i < 16; ++i) wr[i] = wp[(size_t)((C) * 16 + i) * MROWS]; } while (0)
; template <bool RUN_L = true, bool RUN_G = true, bool DRY = false>
; __device__ __forceinline__ void phase_vaccH(unsigned char* ws, LAS unsigned char* lds, int layer, int G) {
;     ...
; #pragma unroll 1
;                 for (int c = 0; c < 8; c += 2) {
;                     VL_LOAD(wb, c + 1);
;                     __builtin_amdgcn_sched_barrier(0);
;                     VL_CHUNK(wa);
;                     __builtin_amdgcn_sched_barrier(0);
;                     VL_LOAD(wa, (c + 2) & 7);
;                     __builtin_amdgcn_sched_barrier(0);
;                     VL_CHUNK(wb);
;                     __builtin_amdgcn_sched_barrier(0);
;                 }
;                 if (valid) { hp[0] = h0 + (f32x4){accf[0], accf[1], accf[2], accf[3]}; hp[1] = h1 + (f32x4){accf[4], accf[5], accf[6], accf[7]}; }
	v_perm_b32 v110, 0, v62, v169
	v_perm_b32 v62, 0, v62, v170
	v_perm_b32 v111, 0, v63, v169
	v_perm_b32 v63, 0, v63, v170
	v_pk_fma_f16 v28, v90, v108, v28
	v_pk_fma_f16 v29, v90, v60, v29
	v_pk_fma_f16 v30, v90, v109, v30
	v_pk_fma_f16 v31, v90, v61, v31
	s_waitcnt lgkmcnt(7)
	v_perm_b32 v112, 0, v64, v169
	v_perm_b32 v64, 0, v64, v170
	v_perm_b32 v113, 0, v65, v169
	v_perm_b32 v65, 0, v65, v170
	v_pk_fma_f16 v28, v91, v110, v28
	v_pk_fma_f16 v29, v91, v62, v29
	v_pk_fma_f16 v30, v91, v111, v30
	v_pk_fma_f16 v31, v91, v63, v31
	s_waitcnt lgkmcnt(6)
	v_perm_b32 v114, 0, v66, v169
	v_perm_b32 v66, 0, v66, v170
	v_perm_b32 v115, 0, v67, v169
	v_perm_b32 v67, 0, v67, v170
	v_pk_fma_f16 v28, v92, v112, v28
	v_pk_fma_f16 v29, v92, v64, v29
	v_pk_fma_f16 v30, v92, v113, v30
	v_pk_fma_f16 v31, v92, v65, v31
	s_waitcnt lgkmcnt(5)
	v_perm_b32 v116, 0, v68, v169
	v_perm_b32 v68, 0, v68, v170
	v_perm_b32 v117, 0, v69, v169
	v_perm_b32 v69, 0, v69, v170
	v_pk_fma_f16 v28, v93, v114, v28
	v_pk_fma_f16 v29, v93, v66, v29
	v_pk_fma_f16 v30, v93, v115, v30
	v_pk_fma_f16 v31, v93, v67, v31
	s_waitcnt lgkmcnt(4)
	v_perm_b32 v118, 0, v70, v169
	v_perm_b32 v70, 0, v70, v170
	v_perm_b32 v119, 0, v71, v169
	v_perm_b32 v71, 0, v71, v170
	v_pk_fma_f16 v28, v94, v116, v28
	v_pk_fma_f16 v29, v94, v68, v29
	v_pk_fma_f16 v30, v94, v117, v30
	v_pk_fma_f16 v31, v94, v69, v31
	s_waitcnt lgkmcnt(3)
	v_perm_b32 v120, 0, v72, v169
	v_perm_b32 v72, 0, v72, v170
	v_perm_b32 v121, 0, v73, v169
	v_perm_b32 v73, 0, v73, v170
	v_pk_fma_f16 v28, v95, v118, v28
	v_pk_fma_f16 v29, v95, v70, v29
	v_pk_fma_f16 v30, v95, v119, v30
	v_pk_fma_f16 v31, v95, v71, v31
	s_waitcnt lgkmcnt(2)
	v_perm_b32 v122, 0, v74, v169
	v_perm_b32 v74, 0, v74, v170
	v_perm_b32 v123, 0, v75, v169
	v_perm_b32 v75, 0, v75, v170
	v_pk_fma_f16 v28, v96, v120, v28
	v_pk_fma_f16 v29, v96, v72, v29
	v_pk_fma_f16 v30, v96, v121, v30
	v_pk_fma_f16 v31, v96, v73, v31
	s_waitcnt lgkmcnt(1)
	v_perm_b32 v124, 0, v76, v169
	v_perm_b32 v76, 0, v76, v170
	v_perm_b32 v125, 0, v77, v169
	v_perm_b32 v77, 0, v77, v170
	v_pk_fma_f16 v28, v97, v122, v28
	v_pk_fma_f16 v29, v97, v74, v29
	v_pk_fma_f16 v30, v97, v123, v30
	v_pk_fma_f16 v31, v97, v75, v31
	s_waitcnt lgkmcnt(0)
	v_perm_b32 v126, 0, v78, v169
	v_perm_b32 v78, 0, v78, v170
	v_perm_b32 v127, 0, v79, v169
	v_perm_b32 v79, 0, v79, v170
	v_pk_fma_f16 v28, v98, v124, v28
	v_pk_fma_f16 v29, v98, v76, v29
	v_pk_fma_f16 v30, v98, v125, v30
	v_pk_fma_f16 v31, v98, v77, v31
	v_pk_fma_f16 v33, v99, v126, v28
	v_pk_fma_f16 v52, v99, v78, v29
	v_pk_fma_f16 v29, v99, v127, v30
	v_pk_fma_f16 v31, v99, v79, v31
	v_cvt_f32_f16_e32 v32, v33
	v_cvt_f32_f16_e32 v30, v52
	v_cvt_f32_f16_e32 v28, v29
	v_cvt_f32_f16_e32 v34, v31
	v_cvt_f32_f16_sdwa v35, v31 dst_sel:DWORD dst_unused:UNUSED_PAD src0_sel:WORD_1
	v_cvt_f32_f16_sdwa v29, v29 dst_sel:DWORD dst_unused:UNUSED_PAD src0_sel:WORD_1
	v_cvt_f32_f16_sdwa v31, v52 dst_sel:DWORD dst_unused:UNUSED_PAD src0_sel:WORD_1
	v_cvt_f32_f16_sdwa v33, v33 dst_sel:DWORD dst_unused:UNUSED_PAD src0_sel:WORD_1
	v_pk_add_f32 v[80:81], v[18:19], v[24:25]
	v_pk_add_f32 v[82:83], v[16:17], v[26:27]
	v_pk_add_f32 v[20:21], v[20:21], v[34:35]
	v_pk_add_f32 v[22:23], v[22:23], v[28:29]
	v_pk_add_f32 v[34:35], v[82:83], v[30:31]
	v_pk_add_f32 v[28:29], v[80:81], v[32:33]
	s_add_u32 s76, s76, s20
	s_addc_u32 s77, s77, s21
	s_add_i32 s46, s46, 32
	s_add_i32 s47, s47, 2
	s_cmp_lt_u32 s47, 6
	v_lshl_add_u64 v[14:15], v[14:15], 0, s[20:21]
	s_cbranch_scc1 .LBB0_1242
	s_and_saveexec_b64 s[46:47], s[6:7]
	s_cbranch_execz .LBB0_1240
	v_pk_add_f32 v[12:13], v[18:19], v[24:25]
	v_pk_add_f32 v[14:15], v[16:17], v[26:27]
	v_pk_add_f32 v[12:13], v[12:13], v[32:33]
	v_pk_add_f32 v[14:15], v[14:15], v[30:31]
	v_pk_add_f32 v[6:7], v[6:7], v[12:13]
	v_pk_add_f32 v[8:9], v[8:9], v[14:15]
	v_pk_add_f32 v[4:5], v[4:5], v[20:21]
	v_pk_add_f32 v[2:3], v[2:3], v[22:23]
	global_store_dwordx4 v[10:11], v[6:9], off
	global_store_dwordx4 v[10:11], v[2:5], off offset:16
	s_branch .LBB0_1240

; #define VL_LOAD(wr, C) do { _Pragma("unroll") for (int i = 0; i < 16; ++i) wr[i] = wp[(size_t)((C) * 16 + i) * MROWS]; } while (0)
; #define VL_LOAD(wr, C) do { _Pragma("unroll") for (int i = 0; i < 16; ++i) wr[i] = wp[(size_t)((C) * 16 + i) * MROWS]; } while (0)
; template <bool RUN_L = true, bool RUN_G = true, bool DRY = false>
; __device__ __forceinline__ void phase_vaccH(unsigned char* ws, LAS unsigned char* lds, int layer, int G) {
;     ...
;                 VL_LOAD(wa, 0);
; #pragma unroll 1
;                 for (int c = 0; c < 8; c += 2) {
;                     VL_LOAD(wb, c + 1);
;                     __builtin_amdgcn_sched_barrier(0);
;                     VL_CHUNK(wa);
.LBB0_1987:
	s_add_u32 s78, s76, s52
	s_addc_u32 s79, s77, 0
	global_load_dword v72, v238, s[78:79] offset:64
	s_add_u32 s78, s76, s41
	s_addc_u32 s79, s77, 0
	global_load_dword v73, v238, s[78:79] offset:128
	s_add_u32 s78, s76, s45
	s_addc_u32 s79, s77, 0
	global_load_dword v74, v238, s[78:79] offset:192
	s_add_u32 s78, s76, s54
	s_addc_u32 s79, s77, 0
	global_load_dword v75, v238, s[78:79] offset:256
	s_add_u32 s78, s76, s55
	s_addc_u32 s79, s77, 0
	global_load_dword v76, v238, s[78:79] offset:320
	s_add_u32 s78, s76, s56
	s_addc_u32 s79, s77, 0
	global_load_dword v77, v238, s[78:79] offset:384
	s_add_u32 s78, s76, s57
	s_addc_u32 s79, s77, 0
	global_load_dword v78, v238, s[78:79] offset:448
	s_add_u32 s78, s76, s58
	s_addc_u32 s79, s77, 0
	global_load_dword v79, v238, s[78:79] offset:512
	global_load_dword v80, v238, s[76:77]
	s_add_u32 s78, s76, s59
	s_addc_u32 s79, s77, 0
	global_load_dword v81, v238, s[78:79] offset:576
	s_add_u32 s78, s76, s60
	s_addc_u32 s79, s77, 0
	global_load_dword v82, v238, s[78:79] offset:640
	s_add_u32 s78, s76, s61
	s_addc_u32 s79, s77, 0
	global_load_dword v83, v238, s[78:79] offset:704
	s_add_u32 s78, s76, s62
	s_addc_u32 s79, s77, 0
	global_load_dword v84, v238, s[78:79] offset:768
	s_add_u32 s78, s76, s63
	s_addc_u32 s79, s77, 0
	global_load_dword v85, v238, s[78:79] offset:832
	s_add_u32 s78, s76, s64
	s_addc_u32 s79, s77, 0
	global_load_dword v86, v238, s[78:79] offset:896
	s_add_u32 s78, s76, s65
	s_addc_u32 s79, s77, 0
	global_load_dword v87, v238, s[78:79] offset:960
	v_mov_b32_e32 v17, v31
	v_mov_b32_e32 v16, v30
	v_mov_b32_e32 v19, v29
	v_mov_b32_e32 v18, v28
	s_waitcnt vmcnt(30)
	v_lshlrev_b32_sdwa v26, v239, v44 dst_sel:DWORD dst_unused:UNUSED_PAD src0_sel:DWORD src1_sel:WORD_1
	s_waitcnt vmcnt(29)
	v_lshlrev_b32_sdwa v28, v239, v42 dst_sel:DWORD dst_unused:UNUSED_PAD src0_sel:DWORD src1_sel:WORD_1
	s_waitcnt vmcnt(28)
	v_lshlrev_b32_sdwa v24, v239, v46 dst_sel:DWORD dst_unused:UNUSED_PAD src0_sel:DWORD src1_sel:WORD_1
	v_lshlrev_b32_sdwa v30, v239, v40 dst_sel:DWORD dst_unused:UNUSED_PAD src0_sel:DWORD src1_sel:WORD_1
	ds_read_b64 v[24:25], v24
	ds_read_b64 v[26:27], v26
	ds_read_b64 v[28:29], v28
	ds_read_b64 v[30:31], v30
	v_perm_b32 v46, v46, v46, s53
	s_waitcnt lgkmcnt(3)
	v_perm_b32 v88, 0, v24, v169
	v_perm_b32 v24, 0, v24, v170
	v_perm_b32 v89, 0, v25, v169
	v_perm_b32 v25, 0, v25, v170
	v_pk_fma_f16 v88, v46, v88, 0
	v_pk_fma_f16 v24, v46, v24, 0
	v_pk_fma_f16 v89, v46, v89, 0
	v_pk_fma_f16 v25, v46, v25, 0
	v_perm_b32 v44, v44, v44, s53
	s_waitcnt lgkmcnt(2)
	v_perm_b32 v46, 0, v26, v169
	v_perm_b32 v26, 0, v26, v170
	v_pk_fma_f16 v24, v44, v26, v24
	v_perm_b32 v26, 0, v27, v169
	v_perm_b32 v27, 0, v27, v170
	s_waitcnt vmcnt(26)
	v_pk_fma_f16 v25, v44, v27, v25
	v_perm_b32 v27, v42, v42, s53
	s_waitcnt lgkmcnt(1)
	v_perm_b32 v42, 0, v28, v169
	v_perm_b32 v28, 0, v28, v170
	v_lshlrev_b32_sdwa v34, v239, v38 dst_sel:DWORD dst_unused:UNUSED_PAD src0_sel:DWORD src1_sel:WORD_1
	s_waitcnt vmcnt(25)
	v_pk_fma_f16 v26, v44, v26, v89
	v_pk_fma_f16 v24, v27, v28, v24
	v_perm_b32 v28, 0, v29, v169
	v_lshlrev_b32_sdwa v52, v239, v37 dst_sel:DWORD dst_unused:UNUSED_PAD src0_sel:DWORD src1_sel:WORD_1
	s_waitcnt vmcnt(24)
	v_pk_fma_f16 v46, v44, v46, v88
	v_pk_fma_f16 v26, v27, v28, v26
	v_perm_b32 v28, 0, v29, v170
	v_lshlrev_b32_sdwa v32, v239, v39 dst_sel:DWORD dst_unused:UNUSED_PAD src0_sel:DWORD src1_sel:WORD_1
	v_lshlrev_b32_sdwa v54, v239, v36 dst_sel:DWORD dst_unused:UNUSED_PAD src0_sel:DWORD src1_sel:WORD_1
	v_pk_fma_f16 v42, v27, v42, v46
	v_pk_fma_f16 v25, v27, v28, v25
	v_perm_b32 v27, v40, v40, s53
	s_waitcnt lgkmcnt(0)
	v_perm_b32 v29, 0, v30, v170
	ds_read_b64 v[32:33], v32
	ds_read_b64 v[34:35], v34
	ds_read_b64 v[52:53], v52
	ds_read_b64 v[54:55], v54
	v_pk_fma_f16 v24, v27, v29, v24
	v_perm_b32 v29, 0, v31, v169
	v_perm_b32 v28, 0, v30, v169
	v_pk_fma_f16 v26, v27, v29, v26
	v_perm_b32 v29, 0, v31, v170
	v_pk_fma_f16 v28, v27, v28, v42
	v_pk_fma_f16 v25, v27, v29, v25
	v_perm_b32 v27, v39, v39, s53
	s_waitcnt lgkmcnt(3)
	v_perm_b32 v29, 0, v32, v169
	v_pk_fma_f16 v28, v27, v29, v28
	v_perm_b32 v29, 0, v32, v170
	v_pk_fma_f16 v24, v27, v29, v24
	v_perm_b32 v29, 0, v33, v169
	v_pk_fma_f16 v26, v27, v29, v26
	v_perm_b32 v29, 0, v33, v170
	v_pk_fma_f16 v25, v27, v29, v25
	v_perm_b32 v27, v38, v38, s53
	s_waitcnt lgkmcnt(2)
	v_perm_b32 v29, 0, v34, v169
	v_pk_fma_f16 v28, v27, v29, v28
	v_perm_b32 v29, 0, v34, v170
	v_pk_fma_f16 v24, v27, v29, v24
	v_perm_b32 v29, 0, v35, v169
	v_pk_fma_f16 v26, v27, v29, v26
	v_perm_b32 v29, 0, v35, v170
	v_pk_fma_f16 v25, v27, v29, v25
	v_perm_b32 v27, v37, v37, s53
	s_waitcnt lgkmcnt(1)
	v_perm_b32 v29, 0, v52, v169
	v_pk_fma_f16 v28, v27, v29, v28
	v_perm_b32 v29, 0, v52, v170
	s_waitcnt vmcnt(22)
	v_pk_fma_f16 v24, v27, v29, v24
	v_perm_b32 v29, 0, v53, v169
	v_lshlrev_b32_sdwa v58, v239, v50 dst_sel:DWORD dst_unused:UNUSED_PAD src0_sel:DWORD src1_sel:WORD_1
	s_waitcnt vmcnt(21)
	v_pk_fma_f16 v26, v27, v29, v26
	v_perm_b32 v29, 0, v53, v170
	v_lshlrev_b32_sdwa v60, v239, v49 dst_sel:DWORD dst_unused:UNUSED_PAD src0_sel:DWORD src1_sel:WORD_1
	s_waitcnt vmcnt(20)
	v_pk_fma_f16 v25, v27, v29, v25
	v_perm_b32 v27, v36, v36, s53
	s_waitcnt lgkmcnt(0)
	v_perm_b32 v29, 0, v54, v169
	v_lshlrev_b32_sdwa v56, v239, v51 dst_sel:DWORD dst_unused:UNUSED_PAD src0_sel:DWORD src1_sel:WORD_1
	v_lshlrev_b32_sdwa v62, v239, v48 dst_sel:DWORD dst_unused:UNUSED_PAD src0_sel:DWORD src1_sel:WORD_1
	v_pk_fma_f16 v28, v27, v29, v28
	v_perm_b32 v29, 0, v54, v170
	ds_read_b64 v[56:57], v56
	ds_read_b64 v[58:59], v58
	ds_read_b64 v[60:61], v60
	ds_read_b64 v[62:63], v62
	v_pk_fma_f16 v24, v27, v29, v24
	v_perm_b32 v29, 0, v55, v169
	v_pk_fma_f16 v26, v27, v29, v26
	v_perm_b32 v29, 0, v55, v170
	v_pk_fma_f16 v25, v27, v29, v25
	v_perm_b32 v27, v51, v51, s53
	s_waitcnt lgkmcnt(3)
; #define VL_LOAD(wr, C) do { _Pragma("unroll") for (int i = 0; i < 16; ++i) wr[i] = wp[(size_t)((C) * 16 + i) * MROWS]; } while (0)
; #define VL_LOAD(wr, C) do { _Pragma("unroll") for (int i = 0; i < 16; ++i) wr[i] = wp[(size_t)((C) * 16 + i) * MROWS]; } while (0)
; template <bool RUN_L = true, bool RUN_G = true, bool DRY = false>
; __device__ __forceinline__ void phase_vaccH(unsigned char* ws, LAS unsigned char* lds, int layer, int G) {
;     ...
;                     VL_LOAD(wa, (c + 2) & 7);
	v_perm_b32 v29, 0, v56, v169
	v_pk_fma_f16 v28, v27, v29, v28
	v_perm_b32 v29, 0, v56, v170
	v_pk_fma_f16 v24, v27, v29, v24
	v_perm_b32 v29, 0, v57, v169
	v_pk_fma_f16 v26, v27, v29, v26
	v_perm_b32 v29, 0, v57, v170
	v_pk_fma_f16 v25, v27, v29, v25
	v_perm_b32 v27, v50, v50, s53
	s_waitcnt lgkmcnt(2)
	v_perm_b32 v29, 0, v58, v169
	v_pk_fma_f16 v28, v27, v29, v28
	v_perm_b32 v29, 0, v58, v170
	v_pk_fma_f16 v24, v27, v29, v24
	v_perm_b32 v29, 0, v59, v169
	v_pk_fma_f16 v26, v27, v29, v26
	v_perm_b32 v29, 0, v59, v170
	v_pk_fma_f16 v25, v27, v29, v25
	v_perm_b32 v27, v49, v49, s53
	s_waitcnt lgkmcnt(1)
	v_perm_b32 v29, 0, v60, v169
	v_pk_fma_f16 v28, v27, v29, v28
	v_perm_b32 v29, 0, v60, v170
	s_waitcnt vmcnt(18)
	v_pk_fma_f16 v24, v27, v29, v24
	v_perm_b32 v29, 0, v61, v169
	v_lshlrev_b32_sdwa v66, v239, v45 dst_sel:DWORD dst_unused:UNUSED_PAD src0_sel:DWORD src1_sel:WORD_1
	s_waitcnt vmcnt(17)
	v_pk_fma_f16 v26, v27, v29, v26
	v_perm_b32 v29, 0, v61, v170
	v_lshlrev_b32_sdwa v68, v239, v43 dst_sel:DWORD dst_unused:UNUSED_PAD src0_sel:DWORD src1_sel:WORD_1
	s_waitcnt vmcnt(16)
	v_pk_fma_f16 v25, v27, v29, v25
	v_perm_b32 v27, v48, v48, s53
	s_waitcnt lgkmcnt(0)
	v_perm_b32 v29, 0, v62, v169
	v_lshlrev_b32_sdwa v64, v239, v47 dst_sel:DWORD dst_unused:UNUSED_PAD src0_sel:DWORD src1_sel:WORD_1
	v_lshlrev_b32_sdwa v70, v239, v41 dst_sel:DWORD dst_unused:UNUSED_PAD src0_sel:DWORD src1_sel:WORD_1
	v_pk_fma_f16 v28, v27, v29, v28
	v_perm_b32 v29, 0, v62, v170
	ds_read_b64 v[64:65], v64
	ds_read_b64 v[66:67], v66
	ds_read_b64 v[68:69], v68
	ds_read_b64 v[70:71], v70
	v_pk_fma_f16 v24, v27, v29, v24
	v_perm_b32 v29, 0, v63, v169
	v_pk_fma_f16 v26, v27, v29, v26
	v_perm_b32 v29, 0, v63, v170
	v_pk_fma_f16 v25, v27, v29, v25
	v_perm_b32 v27, v47, v47, s53
	s_waitcnt lgkmcnt(3)
	v_perm_b32 v29, 0, v64, v169
	v_pk_fma_f16 v28, v27, v29, v28
	v_perm_b32 v29, 0, v64, v170
	v_pk_fma_f16 v24, v27, v29, v24
	v_perm_b32 v29, 0, v65, v169
	v_pk_fma_f16 v26, v27, v29, v26
	v_perm_b32 v29, 0, v65, v170
	v_pk_fma_f16 v25, v27, v29, v25
	v_perm_b32 v27, v45, v45, s53
	s_waitcnt lgkmcnt(2)
	v_perm_b32 v29, 0, v66, v169
	v_pk_fma_f16 v28, v27, v29, v28
	v_perm_b32 v29, 0, v66, v170
	v_pk_fma_f16 v24, v27, v29, v24
	v_perm_b32 v29, 0, v67, v169
	v_pk_fma_f16 v26, v27, v29, v26
	v_perm_b32 v29, 0, v67, v170
	v_pk_fma_f16 v25, v27, v29, v25
	v_perm_b32 v27, v43, v43, s53
	s_waitcnt lgkmcnt(1)
	v_perm_b32 v29, 0, v68, v169
	v_pk_fma_f16 v28, v27, v29, v28
	v_perm_b32 v29, 0, v68, v170
	v_pk_fma_f16 v24, v27, v29, v24
	v_perm_b32 v29, 0, v69, v169
	v_pk_fma_f16 v26, v27, v29, v26
	v_perm_b32 v29, 0, v69, v170
	v_pk_fma_f16 v25, v27, v29, v25
	v_perm_b32 v27, v41, v41, s53
	s_waitcnt lgkmcnt(0)
	v_perm_b32 v29, 0, v70, v169
	v_pk_fma_f16 v56, v27, v29, v28
	v_perm_b32 v28, 0, v70, v170
	v_pk_fma_f16 v57, v27, v28, v24
	v_perm_b32 v24, 0, v71, v169
	v_pk_fma_f16 v58, v27, v24, v26
	v_perm_b32 v24, 0, v71, v170
	v_pk_fma_f16 v59, v27, v24, v25
	s_and_b32 s8, s30, 0x60
	s_mul_i32 s8, s8, 0x8040
	s_add_u32 s98, s16, s8
	s_addc_u32 s99, s17, 0
	global_load_dword v46, v238, s[98:99]
	s_add_u32 s78, s98, s52
	s_addc_u32 s79, s99, 0
	global_load_dword v44, v238, s[78:79] offset:64
	s_add_u32 s78, s98, s41
	s_addc_u32 s79, s99, 0
	global_load_dword v42, v238, s[78:79] offset:128
	s_add_u32 s78, s98, s45
	s_addc_u32 s79, s99, 0
	global_load_dword v40, v238, s[78:79] offset:192
	s_add_u32 s78, s98, s54
	s_addc_u32 s79, s99, 0
	global_load_dword v39, v238, s[78:79] offset:256
	s_add_u32 s78, s98, s55
	s_addc_u32 s79, s99, 0
	global_load_dword v38, v238, s[78:79] offset:320
	s_add_u32 s78, s98, s56
	s_addc_u32 s79, s99, 0
	global_load_dword v37, v238, s[78:79] offset:384
	s_add_u32 s78, s98, s57
	s_addc_u32 s79, s99, 0
	global_load_dword v36, v238, s[78:79] offset:448
	s_add_u32 s78, s98, s58
	s_addc_u32 s79, s99, 0
	global_load_dword v51, v238, s[78:79] offset:512
	s_add_u32 s78, s98, s59
	s_addc_u32 s79, s99, 0
	global_load_dword v50, v238, s[78:79] offset:576
	s_add_u32 s78, s98, s60
	s_addc_u32 s79, s99, 0
	global_load_dword v49, v238, s[78:79] offset:640
	s_add_u32 s78, s98, s61
	s_addc_u32 s79, s99, 0
	global_load_dword v48, v238, s[78:79] offset:704
	s_add_u32 s78, s98, s62
	s_addc_u32 s79, s99, 0
	global_load_dword v47, v238, s[78:79] offset:768
	s_add_u32 s78, s98, s63
	s_addc_u32 s79, s99, 0
	global_load_dword v45, v238, s[78:79] offset:832
	s_add_u32 s78, s98, s64
	s_addc_u32 s79, s99, 0
	global_load_dword v43, v238, s[78:79] offset:896
	s_add_u32 s78, s98, s65
	s_addc_u32 s79, s99, 0
	global_load_dword v41, v238, s[78:79] offset:960
	v_cvt_f32_f16_e32 v28, v58
	v_cvt_f32_f16_sdwa v29, v58 dst_sel:DWORD dst_unused:UNUSED_PAD src0_sel:WORD_1
	v_cvt_f32_f16_e32 v30, v59
	v_cvt_f32_f16_sdwa v31, v59 dst_sel:DWORD dst_unused:UNUSED_PAD src0_sel:WORD_1
	s_waitcnt vmcnt(23)
	s_waitcnt vmcnt(22)
	s_waitcnt vmcnt(21)
	s_waitcnt vmcnt(20)
	s_waitcnt vmcnt(19)
	s_waitcnt vmcnt(18)
	s_waitcnt vmcnt(17)
	s_waitcnt vmcnt(16)
	v_perm_b32 v89, v72, v72, s53
	v_perm_b32 v90, v73, v73, s53
	v_perm_b32 v91, v74, v74, s53
	v_perm_b32 v92, v75, v75, s53
	v_perm_b32 v93, v76, v76, s53
	v_perm_b32 v94, v77, v77, s53
	v_perm_b32 v95, v78, v78, s53
	v_cvt_f32_f16_e32 v24, v56
	v_cvt_f32_f16_sdwa v25, v56 dst_sel:DWORD dst_unused:UNUSED_PAD src0_sel:WORD_1
	v_cvt_f32_f16_e32 v26, v57
	v_cvt_f32_f16_sdwa v27, v57 dst_sel:DWORD dst_unused:UNUSED_PAD src0_sel:WORD_1
	v_lshlrev_b32_sdwa v32, v239, v80 dst_sel:DWORD dst_unused:UNUSED_PAD src0_sel:DWORD src1_sel:WORD_1
	v_lshlrev_b32_sdwa v56, v239, v72 dst_sel:DWORD dst_unused:UNUSED_PAD src0_sel:DWORD src1_sel:WORD_1
	v_lshlrev_b32_sdwa v57, v239, v73 dst_sel:DWORD dst_unused:UNUSED_PAD src0_sel:DWORD src1_sel:WORD_1
	v_lshlrev_b32_sdwa v58, v239, v74 dst_sel:DWORD dst_unused:UNUSED_PAD src0_sel:DWORD src1_sel:WORD_1
	v_lshlrev_b32_sdwa v59, v239, v75 dst_sel:DWORD dst_unused:UNUSED_PAD src0_sel:DWORD src1_sel:WORD_1
	v_lshlrev_b32_sdwa v68, v239, v76 dst_sel:DWORD dst_unused:UNUSED_PAD src0_sel:DWORD src1_sel:WORD_1
	v_lshlrev_b32_sdwa v69, v239, v77 dst_sel:DWORD dst_unused:UNUSED_PAD src0_sel:DWORD src1_sel:WORD_1
	v_lshlrev_b32_sdwa v70, v239, v78 dst_sel:DWORD dst_unused:UNUSED_PAD src0_sel:DWORD src1_sel:WORD_1
	v_lshlrev_b32_sdwa v71, v239, v79 dst_sel:DWORD dst_unused:UNUSED_PAD src0_sel:DWORD src1_sel:WORD_1
	v_lshlrev_b32_sdwa v72, v239, v81 dst_sel:DWORD dst_unused:UNUSED_PAD src0_sel:DWORD src1_sel:WORD_1
	v_lshlrev_b32_sdwa v73, v239, v82 dst_sel:DWORD dst_unused:UNUSED_PAD src0_sel:DWORD src1_sel:WORD_1
	v_lshlrev_b32_sdwa v74, v239, v83 dst_sel:DWORD dst_unused:UNUSED_PAD src0_sel:DWORD src1_sel:WORD_1
	v_lshlrev_b32_sdwa v75, v239, v84 dst_sel:DWORD dst_unused:UNUSED_PAD src0_sel:DWORD src1_sel:WORD_1
	v_lshlrev_b32_sdwa v76, v239, v85 dst_sel:DWORD dst_unused:UNUSED_PAD src0_sel:DWORD src1_sel:WORD_1
	v_lshlrev_b32_sdwa v77, v239, v86 dst_sel:DWORD dst_unused:UNUSED_PAD src0_sel:DWORD src1_sel:WORD_1
	v_lshlrev_b32_sdwa v78, v239, v87 dst_sel:DWORD dst_unused:UNUSED_PAD src0_sel:DWORD src1_sel:WORD_1
	v_perm_b32 v88, v80, v80, s53
	v_perm_b32 v96, v79, v79, s53
	ds_read_b64 v[32:33], v32
	ds_read_b64 v[34:35], v56
	ds_read_b64 v[52:53], v57
	ds_read_b64 v[54:55], v58
	ds_read_b64 v[56:57], v59
	ds_read_b64 v[58:59], v68
	ds_read_b64 v[60:61], v69
	ds_read_b64 v[62:63], v70
	ds_read_b64 v[64:65], v71
	ds_read_b64 v[66:67], v72
	ds_read_b64 v[68:69], v73
	ds_read_b64 v[70:71], v74
	ds_read_b64 v[72:73], v75
	ds_read_b64 v[74:75], v76
	ds_read_b64 v[76:77], v77
	ds_read_b64 v[78:79], v78
	v_pk_add_f32 v[22:23], v[22:23], v[28:29]
	v_pk_add_f32 v[20:21], v[20:21], v[30:31]
	s_waitcnt lgkmcnt(14)
	v_perm_b32 v28, 0, v32, v169
	v_perm_b32 v29, 0, v32, v170
	v_perm_b32 v30, 0, v33, v169
	v_perm_b32 v31, 0, v33, v170
	v_perm_b32 v32, 0, v34, v169
	v_perm_b32 v33, 0, v34, v170
	v_perm_b32 v34, 0, v35, v169
	v_perm_b32 v35, 0, v35, v170
	v_pk_fma_f16 v28, v88, v28, 0
	v_pk_fma_f16 v29, v88, v29, 0
	v_pk_fma_f16 v30, v88, v30, 0
	v_pk_fma_f16 v31, v88, v31, 0
	s_waitcnt lgkmcnt(13)
	v_perm_b32 v100, 0, v52, v169
	v_perm_b32 v52, 0, v52, v170
	v_perm_b32 v101, 0, v53, v169
	v_perm_b32 v53, 0, v53, v170
	v_pk_fma_f16 v28, v89, v32, v28
	v_pk_fma_f16 v29, v89, v33, v29
	v_pk_fma_f16 v30, v89, v34, v30
	v_pk_fma_f16 v31, v89, v35, v31
	s_waitcnt lgkmcnt(12)
	v_perm_b32 v102, 0, v54, v169
	v_perm_b32 v54, 0, v54, v170
	v_perm_b32 v103, 0, v55, v169
	v_perm_b32 v55, 0, v55, v170
	v_pk_fma_f16 v28, v90, v100, v28
	v_pk_fma_f16 v29, v90, v52, v29
	v_pk_fma_f16 v30, v90, v101, v30
	v_pk_fma_f16 v31, v90, v53, v31
	s_waitcnt lgkmcnt(11)
	v_perm_b32 v104, 0, v56, v169
	v_perm_b32 v56, 0, v56, v170
	v_perm_b32 v105, 0, v57, v169
	v_perm_b32 v57, 0, v57, v170
	v_pk_fma_f16 v28, v91, v102, v28
	v_pk_fma_f16 v29, v91, v54, v29
	v_pk_fma_f16 v30, v91, v103, v30
	v_pk_fma_f16 v31, v91, v55, v31
	s_waitcnt lgkmcnt(10)
	v_perm_b32 v106, 0, v58, v169
	v_perm_b32 v58, 0, v58, v170
	v_perm_b32 v107, 0, v59, v169
	v_perm_b32 v59, 0, v59, v170
	v_pk_fma_f16 v28, v92, v104, v28
	v_pk_fma_f16 v29, v92, v56, v29
	v_pk_fma_f16 v30, v92, v105, v30
	v_pk_fma_f16 v31, v92, v57, v31
	s_waitcnt lgkmcnt(9)
	v_perm_b32 v108, 0, v60, v169
	v_perm_b32 v60, 0, v60, v170
	v_perm_b32 v109, 0, v61, v169
	v_perm_b32 v61, 0, v61, v170
	v_pk_fma_f16 v28, v93, v106, v28
	v_pk_fma_f16 v29, v93, v58, v29
	v_pk_fma_f16 v30, v93, v107, v30
	v_pk_fma_f16 v31, v93, v59, v31
	s_waitcnt lgkmcnt(8)
; #define VL_LOAD(wr, C) do { _Pragma("unroll") for (int i = 0; i < 16; ++i) wr[i] = wp[(size_t)((C) * 16 + i) * MROWS]; } while (0)
; #define VL_LOAD(wr, C) do { _Pragma("unroll") for (int i = 0; i < 16; ++i) wr[i] = wp[(size_t)((C) * 16 + i) * MROWS]; } while (0)
; template <bool RUN_L = true, bool RUN_G = true, bool DRY = false>
; __device__ __forceinline__ void phase_vaccH(unsigned char* ws, LAS unsigned char* lds, int layer, int G) {
;     ...
; #pragma unroll 1
;                 for (int c = 0; c < 8; c += 2) {
;                     VL_LOAD(wb, c + 1);
;                     __builtin_amdgcn_sched_barrier(0);
;                     VL_CHUNK(wa);
;                     __builtin_amdgcn_sched_barrier(0);
;                     VL_LOAD(wa, (c + 2) & 7);
;                     __builtin_amdgcn_sched_barrier(0);
;                     VL_CHUNK(wb);
;                     __builtin_amdgcn_sched_barrier(0);
;                 }
;                 if (valid) { hp[0] = h0 + (f32x4){accf[0], accf[1], accf[2], accf[3]}; hp[1] = h1 + (f32x4){accf[4], accf[5], accf[6], accf[7]}; }
	v_perm_b32 v110, 0, v62, v169
	v_perm_b32 v62, 0, v62, v170
	v_perm_b32 v111, 0, v63, v169
	v_perm_b32 v63, 0, v63, v170
	v_pk_fma_f16 v28, v94, v108, v28
	v_pk_fma_f16 v29, v94, v60, v29
	v_pk_fma_f16 v30, v94, v109, v30
	v_pk_fma_f16 v31, v94, v61, v31
	s_waitcnt lgkmcnt(7)
	v_perm_b32 v112, 0, v64, v169
	v_perm_b32 v64, 0, v64, v170
	v_perm_b32 v113, 0, v65, v169
	v_perm_b32 v65, 0, v65, v170
	v_pk_fma_f16 v28, v95, v110, v28
	v_pk_fma_f16 v29, v95, v62, v29
	v_pk_fma_f16 v30, v95, v111, v30
	v_pk_fma_f16 v31, v95, v63, v31
	v_perm_b32 v97, v81, v81, s53
	s_waitcnt lgkmcnt(6)
	v_perm_b32 v114, 0, v66, v169
	v_perm_b32 v66, 0, v66, v170
	v_perm_b32 v115, 0, v67, v169
	v_perm_b32 v67, 0, v67, v170
	v_pk_fma_f16 v28, v96, v112, v28
	v_pk_fma_f16 v29, v96, v64, v29
	v_pk_fma_f16 v30, v96, v113, v30
	v_pk_fma_f16 v31, v96, v65, v31
	v_perm_b32 v98, v82, v82, s53
	s_waitcnt lgkmcnt(5)
	v_perm_b32 v116, 0, v68, v169
	v_perm_b32 v68, 0, v68, v170
	v_perm_b32 v117, 0, v69, v169
	v_perm_b32 v69, 0, v69, v170
	v_pk_fma_f16 v28, v97, v114, v28
	v_pk_fma_f16 v29, v97, v66, v29
	v_pk_fma_f16 v30, v97, v115, v30
	v_pk_fma_f16 v31, v97, v67, v31
	v_perm_b32 v99, v83, v83, s53
	s_waitcnt lgkmcnt(4)
	v_perm_b32 v118, 0, v70, v169
	v_perm_b32 v70, 0, v70, v170
	v_perm_b32 v119, 0, v71, v169
	v_perm_b32 v71, 0, v71, v170
	v_pk_fma_f16 v28, v98, v116, v28
	v_pk_fma_f16 v29, v98, v68, v29
	v_pk_fma_f16 v30, v98, v117, v30
	v_pk_fma_f16 v31, v98, v69, v31
	v_perm_b32 v84, v84, v84, s53
	s_waitcnt lgkmcnt(3)
	v_perm_b32 v120, 0, v72, v169
	v_perm_b32 v72, 0, v72, v170
	v_perm_b32 v121, 0, v73, v169
	v_perm_b32 v73, 0, v73, v170
	v_pk_fma_f16 v28, v99, v118, v28
	v_pk_fma_f16 v29, v99, v70, v29
	v_pk_fma_f16 v30, v99, v119, v30
	v_pk_fma_f16 v31, v99, v71, v31
	v_perm_b32 v85, v85, v85, s53
	s_waitcnt lgkmcnt(2)
	v_perm_b32 v122, 0, v74, v169
	v_perm_b32 v74, 0, v74, v170
	v_perm_b32 v123, 0, v75, v169
	v_perm_b32 v75, 0, v75, v170
	v_pk_fma_f16 v28, v84, v120, v28
	v_pk_fma_f16 v29, v84, v72, v29
	v_pk_fma_f16 v30, v84, v121, v30
	v_pk_fma_f16 v31, v84, v73, v31
	v_perm_b32 v86, v86, v86, s53
	s_waitcnt lgkmcnt(1)
	v_perm_b32 v124, 0, v76, v169
	v_perm_b32 v76, 0, v76, v170
	v_perm_b32 v125, 0, v77, v169
	v_perm_b32 v77, 0, v77, v170
	v_pk_fma_f16 v28, v85, v122, v28
	v_pk_fma_f16 v29, v85, v74, v29
	v_pk_fma_f16 v30, v85, v123, v30
	v_pk_fma_f16 v31, v85, v75, v31
	v_perm_b32 v87, v87, v87, s53
	s_waitcnt lgkmcnt(0)
	v_perm_b32 v126, 0, v78, v169
	v_perm_b32 v78, 0, v78, v170
	v_perm_b32 v127, 0, v79, v169
	v_perm_b32 v79, 0, v79, v170
	v_pk_fma_f16 v28, v86, v124, v28
	v_pk_fma_f16 v29, v86, v76, v29
	v_pk_fma_f16 v30, v86, v125, v30
	v_pk_fma_f16 v31, v86, v77, v31
	v_pk_fma_f16 v35, v87, v126, v28
	v_pk_fma_f16 v33, v87, v78, v29
	v_pk_fma_f16 v29, v87, v127, v30
	v_pk_fma_f16 v31, v87, v79, v31
	v_cvt_f32_f16_e32 v34, v35
	v_cvt_f32_f16_e32 v32, v33
	v_cvt_f32_f16_e32 v28, v29
	v_cvt_f32_f16_e32 v30, v31
	v_cvt_f32_f16_sdwa v31, v31 dst_sel:DWORD dst_unused:UNUSED_PAD src0_sel:WORD_1
	v_cvt_f32_f16_sdwa v29, v29 dst_sel:DWORD dst_unused:UNUSED_PAD src0_sel:WORD_1
	v_cvt_f32_f16_sdwa v33, v33 dst_sel:DWORD dst_unused:UNUSED_PAD src0_sel:WORD_1
	v_cvt_f32_f16_sdwa v35, v35 dst_sel:DWORD dst_unused:UNUSED_PAD src0_sel:WORD_1
	v_pk_add_f32 v[80:81], v[18:19], v[24:25]
	v_pk_add_f32 v[82:83], v[16:17], v[26:27]
	v_pk_add_f32 v[20:21], v[20:21], v[30:31]
	v_pk_add_f32 v[22:23], v[22:23], v[28:29]
	v_pk_add_f32 v[30:31], v[82:83], v[32:33]
	v_pk_add_f32 v[28:29], v[80:81], v[34:35]
	s_add_u32 s76, s76, s20
	s_addc_u32 s77, s77, s21
	s_add_i32 s30, s30, 32
	s_add_i32 s31, s31, 2
	s_cmp_lt_u32 s31, 6
	v_lshl_add_u64 v[14:15], v[14:15], 0, s[20:21]
	s_cbranch_scc1 .LBB0_1987
	s_and_saveexec_b64 s[30:31], s[6:7]
	s_cbranch_execz .LBB0_1985
	v_pk_add_f32 v[12:13], v[18:19], v[24:25]
	v_pk_add_f32 v[14:15], v[16:17], v[26:27]
	v_pk_add_f32 v[12:13], v[12:13], v[34:35]
	v_pk_add_f32 v[14:15], v[14:15], v[32:33]
	v_pk_add_f32 v[6:7], v[6:7], v[12:13]
	v_pk_add_f32 v[8:9], v[8:9], v[14:15]
	v_pk_add_f32 v[4:5], v[4:5], v[20:21]
	v_pk_add_f32 v[2:3], v[2:3], v[22:23]
	global_store_dwordx4 v[10:11], v[6:9], off
	global_store_dwordx4 v[10:11], v[2:5], off offset:16
	s_branch .LBB0_1985
